# mix-out epilogue: the per-row-block sum-of-squares LDS read issued at the top of its block instead of a read + lgkmcnt(0) round trip at the end
# speedup vs baseline: 1.0014x; 1.0014x over previous
; #define PG8_LAS __attribute__((address_space(3)))
; __device__ __forceinline__ unsigned cvt_pk_bf16(float lo, float hi) { const f32x2c v = {lo, hi}; const bf16x2c b = __builtin_convertvector(v, bf16x2c); return __builtin_bit_cast(unsigned, b); }
;     __device__ __forceinline__ void operator()(const f32x4 (&acc)[2][2][4][2], const Unit& u, int wr, int wc, int fr, int fq) const {
;         const int row0 = u.pm * BM + wr * 64 + fr, col0 = u.pn * BM + wc * 32 + 8 * fq;
; #pragma unroll
;         for (int ai = 0; ai < 2; ++ai)
; #pragma unroll
;             for (int m = 0; m < 4; ++m) { const size_t ro = (size_t)(row0 + ai * HALF + m * 16) * D + col0; float q = 0.f;
; #pragma unroll
;                 for (int bj = 0; bj < 2; ++bj) { const f32x4 v0 = acc[ai][bj][m][0] + *(const f32x4*)(R + ro + bj * HALF), v1 = acc[ai][bj][m][1] + *(const f32x4*)(R + ro + bj * HALF + 4);
;                     q += (v0[0] * v0[0] + v0[1] * v0[1]) + (v0[2] * v0[2] + v0[3] * v0[3]) + (v1[0] * v1[0] + v1[1] * v1[1]) + (v1[2] * v1[2] + v1[3] * v1[3]);
;                     u32x4 w; w.x = cvt_pk_bf16(v0[0], v0[1]); w.y = cvt_pk_bf16(v0[2], v0[3]); w.z = cvt_pk_bf16(v1[0], v1[1]); w.w = cvt_pk_bf16(v1[2], v1[3]);
;                     *(u32x4*)(O + ro + bj * HALF) = w; }
;                 q = rows_sum4(q);
;                 if (fq == 0) { PG8_LAS float* sp = ss + (ai * HALF + wr * 64 + m * 16 + fr) * 4 + wc; *sp += q; } }
.LBB0_2039:
	v_lshl_add_u32 v142, s16, 8, v144
	v_lshl_or_b32 v140, s17, 8, v146
	v_ashrrev_i32_e32 v143, 31, v142
	v_ashrrev_i32_e32 v141, 31, v140
	v_lshlrev_b64 v[150:151], 10, v[142:143]
	v_lshl_add_u64 v[142:143], v[150:151], 0, v[140:141]
	v_lshl_add_u64 v[140:141], v[142:143], 2, s[56:57]
	v_lshl_add_u64 v[142:143], v[142:143], 1, s[92:93]
	global_load_dwordx4 v[150:153], v[140:141], off nt
	global_load_dwordx4 v[154:157], v[140:141], off offset:16 nt
	global_load_dwordx4 v[158:161], v[140:141], off offset:512 nt
	global_load_dwordx4 v[162:165], v[140:141], off offset:528 nt
	s_mov_b64 s[98:99], 0x10000
	v_lshl_add_u64 v[202:203], v[140:141], 0, s[98:99]
	global_load_dwordx4 v[166:169], v[202:203], off nt
	global_load_dwordx4 v[170:173], v[202:203], off offset:16 nt
	global_load_dwordx4 v[174:177], v[202:203], off offset:512 nt
	global_load_dwordx4 v[178:181], v[202:203], off offset:528 nt
	s_mov_b64 s[98:99], 0x20000
	v_lshl_add_u64 v[202:203], v[140:141], 0, s[98:99]
	global_load_dwordx4 v[182:185], v[202:203], off nt
	global_load_dwordx4 v[186:189], v[202:203], off offset:16 nt
	global_load_dwordx4 v[190:193], v[202:203], off offset:512 nt
	global_load_dwordx4 v[198:201], v[202:203], off offset:528 nt
	ds_read_b32 v149, v147
	s_waitcnt vmcnt(10)
	v_pk_add_f32 v[152:153], v[126:127], v[152:153]
	v_pk_add_f32 v[150:151], v[124:125], v[150:151]
	v_pk_add_f32 v[156:157], v[122:123], v[156:157]
	v_pk_add_f32 v[154:155], v[120:121], v[154:155]
	v_cvt_pk_bf16_f32 v206, v150, v151
	v_cvt_pk_bf16_f32 v207, v152, v153
	v_cvt_pk_bf16_f32 v208, v154, v155
	v_cvt_pk_bf16_f32 v209, v156, v157
	global_store_dwordx4 v[142:143], v[206:209], off
	v_mul_f32_e32 v151, v151, v151
	v_mul_f32_e32 v153, v153, v153
	v_mul_f32_e32 v155, v155, v155
	v_fmac_f32_e32 v151, v150, v150
	v_fmac_f32_e32 v153, v152, v152
	v_mul_f32_e32 v157, v157, v157
	v_fmac_f32_e32 v155, v154, v154
	v_add_f32_e32 v151, v151, v153
	v_fmac_f32_e32 v157, v156, v156
	v_add_f32_e32 v151, v151, v155
	v_add_f32_e32 v214, v157, v151
	s_waitcnt vmcnt(9)
	v_pk_add_f32 v[160:161], v[118:119], v[160:161]
	v_pk_add_f32 v[158:159], v[116:117], v[158:159]
	v_pk_add_f32 v[164:165], v[114:115], v[164:165]
	v_pk_add_f32 v[162:163], v[112:113], v[162:163]
	v_cvt_pk_bf16_f32 v210, v158, v159
	v_cvt_pk_bf16_f32 v211, v160, v161
	v_cvt_pk_bf16_f32 v212, v162, v163
	v_cvt_pk_bf16_f32 v213, v164, v165
	global_store_dwordx4 v[142:143], v[210:213], off offset:256
	v_mul_f32_e32 v159, v159, v159
	v_mul_f32_e32 v161, v161, v161
	v_mul_f32_e32 v163, v163, v163
	v_fmac_f32_e32 v159, v158, v158
	v_fmac_f32_e32 v161, v160, v160
	v_mul_f32_e32 v165, v165, v165
	v_fmac_f32_e32 v163, v162, v162
	v_add_f32_e32 v159, v159, v161
	v_fmac_f32_e32 v165, v164, v164
	v_add_f32_e32 v159, v159, v163
	v_add_f32_e32 v215, v165, v159
	v_add_f32_e32 v214, v214, v215
	s_mov_b64 s[98:99], 0x30000
	v_lshl_add_u64 v[202:203], v[140:141], 0, s[98:99]
	global_load_dwordx4 v[150:153], v[202:203], off nt
	global_load_dwordx4 v[154:157], v[202:203], off offset:16 nt
	global_load_dwordx4 v[158:161], v[202:203], off offset:512 nt
	global_load_dwordx4 v[162:165], v[202:203], off offset:528 nt
	v_mov_b32_e32 v215, v214
	s_nop 1
	v_permlane16_swap_b32_e32 v214, v215
	v_add_f32_e32 v214, v214, v215
	v_mov_b32_e32 v215, v214
	s_nop 1
	v_permlane32_swap_b32_e32 v214, v215
	s_and_saveexec_b64 s[16:17], s[2:3]
	v_add_f32_e32 v214, v214, v215
	s_waitcnt lgkmcnt(0)
	v_add_f32_e32 v214, v214, v149
	ds_write_b32 v147, v214
	s_or_b64 exec, exec, s[16:17]
	ds_read_b32 v149, v147 offset:256
	s_waitcnt vmcnt(12)
	v_pk_add_f32 v[168:169], v[110:111], v[168:169]
	v_pk_add_f32 v[166:167], v[108:109], v[166:167]
	v_pk_add_f32 v[172:173], v[106:107], v[172:173]
	v_pk_add_f32 v[170:171], v[104:105], v[170:171]
	v_cvt_pk_bf16_f32 v206, v166, v167
	v_cvt_pk_bf16_f32 v207, v168, v169
	v_cvt_pk_bf16_f32 v208, v170, v171
	v_cvt_pk_bf16_f32 v209, v172, v173
	s_mov_b64 s[98:99], 0x8000
	v_lshl_add_u64 v[204:205], v[142:143], 0, s[98:99]
	global_store_dwordx4 v[204:205], v[206:209], off
	v_mul_f32_e32 v167, v167, v167
	v_mul_f32_e32 v169, v169, v169
	v_mul_f32_e32 v171, v171, v171
	v_fmac_f32_e32 v167, v166, v166
	v_fmac_f32_e32 v169, v168, v168
	v_mul_f32_e32 v173, v173, v173
	v_fmac_f32_e32 v171, v170, v170
	v_add_f32_e32 v167, v167, v169
	v_fmac_f32_e32 v173, v172, v172
	v_add_f32_e32 v167, v167, v171
	v_add_f32_e32 v214, v173, v167
	s_waitcnt vmcnt(11)
	v_pk_add_f32 v[176:177], v[102:103], v[176:177]
	v_pk_add_f32 v[174:175], v[100:101], v[174:175]
	v_pk_add_f32 v[180:181], v[98:99], v[180:181]
	v_pk_add_f32 v[178:179], v[96:97], v[178:179]
	v_cvt_pk_bf16_f32 v210, v174, v175
	v_cvt_pk_bf16_f32 v211, v176, v177
	v_cvt_pk_bf16_f32 v212, v178, v179
	v_cvt_pk_bf16_f32 v213, v180, v181
	global_store_dwordx4 v[204:205], v[210:213], off offset:256
	v_mul_f32_e32 v175, v175, v175
	v_mul_f32_e32 v177, v177, v177
	v_mul_f32_e32 v179, v179, v179
	v_fmac_f32_e32 v175, v174, v174
	v_fmac_f32_e32 v177, v176, v176
	v_mul_f32_e32 v181, v181, v181
	v_fmac_f32_e32 v179, v178, v178
	v_add_f32_e32 v175, v175, v177
	v_fmac_f32_e32 v181, v180, v180
	v_add_f32_e32 v175, v175, v179
	v_add_f32_e32 v215, v181, v175
	v_add_f32_e32 v214, v214, v215
	s_mov_b64 s[98:99], 0x80000
	v_lshl_add_u64 v[202:203], v[140:141], 0, s[98:99]
	global_load_dwordx4 v[166:169], v[202:203], off nt
	global_load_dwordx4 v[170:173], v[202:203], off offset:16 nt
	global_load_dwordx4 v[174:177], v[202:203], off offset:512 nt
	global_load_dwordx4 v[178:181], v[202:203], off offset:528 nt
	v_mov_b32_e32 v215, v214
	s_nop 1
	v_permlane16_swap_b32_e32 v214, v215
	v_add_f32_e32 v214, v214, v215
	v_mov_b32_e32 v215, v214
	s_nop 1
	v_permlane32_swap_b32_e32 v214, v215
	s_and_saveexec_b64 s[16:17], s[2:3]
	v_add_f32_e32 v214, v214, v215
	s_waitcnt lgkmcnt(0)
; #define PG8_LAS __attribute__((address_space(3)))
; __device__ __forceinline__ unsigned cvt_pk_bf16(float lo, float hi) { const f32x2c v = {lo, hi}; const bf16x2c b = __builtin_convertvector(v, bf16x2c); return __builtin_bit_cast(unsigned, b); }
;     __device__ __forceinline__ void operator()(const f32x4 (&acc)[2][2][4][2], const Unit& u, int wr, int wc, int fr, int fq) const {
;     ...
;             for (int m = 0; m < 4; ++m) { const size_t ro = (size_t)(row0 + ai * HALF + m * 16) * D + col0; float q = 0.f;
; #pragma unroll
;                 for (int bj = 0; bj < 2; ++bj) { const f32x4 v0 = acc[ai][bj][m][0] + *(const f32x4*)(R + ro + bj * HALF), v1 = acc[ai][bj][m][1] + *(const f32x4*)(R + ro + bj * HALF + 4);
;                     q += (v0[0] * v0[0] + v0[1] * v0[1]) + (v0[2] * v0[2] + v0[3] * v0[3]) + (v1[0] * v1[0] + v1[1] * v1[1]) + (v1[2] * v1[2] + v1[3] * v1[3]);
;                     u32x4 w; w.x = cvt_pk_bf16(v0[0], v0[1]); w.y = cvt_pk_bf16(v0[2], v0[3]); w.z = cvt_pk_bf16(v1[0], v1[1]); w.w = cvt_pk_bf16(v1[2], v1[3]);
;                     *(u32x4*)(O + ro + bj * HALF) = w; }
;                 q = rows_sum4(q);
;                 if (fq == 0) { PG8_LAS float* sp = ss + (ai * HALF + wr * 64 + m * 16 + fr) * 4 + wc; *sp += q; } }
	v_add_f32_e32 v214, v214, v149
	ds_write_b32 v147, v214 offset:256
	s_or_b64 exec, exec, s[16:17]
	ds_read_b32 v149, v147 offset:512
	s_waitcnt vmcnt(14)
	v_pk_add_f32 v[184:185], v[94:95], v[184:185]
	v_pk_add_f32 v[182:183], v[92:93], v[182:183]
	v_pk_add_f32 v[188:189], v[90:91], v[188:189]
	v_pk_add_f32 v[186:187], v[88:89], v[186:187]
	v_cvt_pk_bf16_f32 v206, v182, v183
	v_cvt_pk_bf16_f32 v207, v184, v185
	v_cvt_pk_bf16_f32 v208, v186, v187
	v_cvt_pk_bf16_f32 v209, v188, v189
	s_mov_b64 s[98:99], 0x10000
	v_lshl_add_u64 v[204:205], v[142:143], 0, s[98:99]
	global_store_dwordx4 v[204:205], v[206:209], off
	v_mul_f32_e32 v183, v183, v183
	v_mul_f32_e32 v185, v185, v185
	v_mul_f32_e32 v187, v187, v187
	v_fmac_f32_e32 v183, v182, v182
	v_fmac_f32_e32 v185, v184, v184
	v_mul_f32_e32 v189, v189, v189
	v_fmac_f32_e32 v187, v186, v186
	v_add_f32_e32 v183, v183, v185
	v_fmac_f32_e32 v189, v188, v188
	v_add_f32_e32 v183, v183, v187
	v_add_f32_e32 v214, v189, v183
	s_waitcnt vmcnt(13)
	v_pk_add_f32 v[192:193], v[86:87], v[192:193]
	v_pk_add_f32 v[190:191], v[84:85], v[190:191]
	v_pk_add_f32 v[200:201], v[82:83], v[200:201]
	v_pk_add_f32 v[198:199], v[80:81], v[198:199]
	v_cvt_pk_bf16_f32 v210, v190, v191
	v_cvt_pk_bf16_f32 v211, v192, v193
	v_cvt_pk_bf16_f32 v212, v198, v199
	v_cvt_pk_bf16_f32 v213, v200, v201
	global_store_dwordx4 v[204:205], v[210:213], off offset:256
	v_mul_f32_e32 v191, v191, v191
	v_mul_f32_e32 v193, v193, v193
	v_mul_f32_e32 v199, v199, v199
	v_fmac_f32_e32 v191, v190, v190
	v_fmac_f32_e32 v193, v192, v192
	v_mul_f32_e32 v201, v201, v201
	v_fmac_f32_e32 v199, v198, v198
	v_add_f32_e32 v191, v191, v193
	v_fmac_f32_e32 v201, v200, v200
	v_add_f32_e32 v191, v191, v199
	v_add_f32_e32 v215, v201, v191
	v_add_f32_e32 v214, v214, v215
	s_mov_b64 s[98:99], 0x90000
	v_lshl_add_u64 v[202:203], v[140:141], 0, s[98:99]
	global_load_dwordx4 v[182:185], v[202:203], off nt
	global_load_dwordx4 v[186:189], v[202:203], off offset:16 nt
	global_load_dwordx4 v[190:193], v[202:203], off offset:512 nt
	global_load_dwordx4 v[198:201], v[202:203], off offset:528 nt
	v_mov_b32_e32 v215, v214
	s_nop 1
	v_permlane16_swap_b32_e32 v214, v215
	v_add_f32_e32 v214, v214, v215
	v_mov_b32_e32 v215, v214
	s_nop 1
	v_permlane32_swap_b32_e32 v214, v215
	s_and_saveexec_b64 s[16:17], s[2:3]
	v_add_f32_e32 v214, v214, v215
	s_waitcnt lgkmcnt(0)
	v_add_f32_e32 v214, v214, v149
	ds_write_b32 v147, v214 offset:512
	s_or_b64 exec, exec, s[16:17]
	ds_read_b32 v149, v147 offset:768
	s_waitcnt vmcnt(14)
	v_pk_add_f32 v[152:153], v[78:79], v[152:153]
	v_pk_add_f32 v[150:151], v[76:77], v[150:151]
	v_pk_add_f32 v[156:157], v[74:75], v[156:157]
	v_pk_add_f32 v[154:155], v[72:73], v[154:155]
	v_cvt_pk_bf16_f32 v206, v150, v151
	v_cvt_pk_bf16_f32 v207, v152, v153
	v_cvt_pk_bf16_f32 v208, v154, v155
	v_cvt_pk_bf16_f32 v209, v156, v157
	s_mov_b64 s[98:99], 0x18000
	v_lshl_add_u64 v[204:205], v[142:143], 0, s[98:99]
	global_store_dwordx4 v[204:205], v[206:209], off
	v_mul_f32_e32 v151, v151, v151
	v_mul_f32_e32 v153, v153, v153
	v_mul_f32_e32 v155, v155, v155
	v_fmac_f32_e32 v151, v150, v150
	v_fmac_f32_e32 v153, v152, v152
	v_mul_f32_e32 v157, v157, v157
	v_fmac_f32_e32 v155, v154, v154
	v_add_f32_e32 v151, v151, v153
	v_fmac_f32_e32 v157, v156, v156
	v_add_f32_e32 v151, v151, v155
	v_add_f32_e32 v214, v157, v151
	s_waitcnt vmcnt(13)
	v_pk_add_f32 v[160:161], v[70:71], v[160:161]
	v_pk_add_f32 v[158:159], v[68:69], v[158:159]
	v_pk_add_f32 v[164:165], v[66:67], v[164:165]
	v_pk_add_f32 v[162:163], v[64:65], v[162:163]
	v_cvt_pk_bf16_f32 v210, v158, v159
	v_cvt_pk_bf16_f32 v211, v160, v161
	v_cvt_pk_bf16_f32 v212, v162, v163
	v_cvt_pk_bf16_f32 v213, v164, v165
	global_store_dwordx4 v[204:205], v[210:213], off offset:256
	v_mul_f32_e32 v159, v159, v159
	v_mul_f32_e32 v161, v161, v161
	v_mul_f32_e32 v163, v163, v163
	v_fmac_f32_e32 v159, v158, v158
	v_fmac_f32_e32 v161, v160, v160
	v_mul_f32_e32 v165, v165, v165
	v_fmac_f32_e32 v163, v162, v162
	v_add_f32_e32 v159, v159, v161
	v_fmac_f32_e32 v165, v164, v164
	v_add_f32_e32 v159, v159, v163
	v_add_f32_e32 v215, v165, v159
	v_add_f32_e32 v214, v214, v215
	s_mov_b64 s[98:99], 0xa0000
	v_lshl_add_u64 v[202:203], v[140:141], 0, s[98:99]
	global_load_dwordx4 v[150:153], v[202:203], off nt
	global_load_dwordx4 v[154:157], v[202:203], off offset:16 nt
	global_load_dwordx4 v[158:161], v[202:203], off offset:512 nt
	global_load_dwordx4 v[162:165], v[202:203], off offset:528 nt
	v_mov_b32_e32 v215, v214
	s_nop 1
	v_permlane16_swap_b32_e32 v214, v215
	v_add_f32_e32 v214, v214, v215
	v_mov_b32_e32 v215, v214
	s_nop 1
	v_permlane32_swap_b32_e32 v214, v215
	s_and_saveexec_b64 s[16:17], s[2:3]
	v_add_f32_e32 v214, v214, v215
	s_waitcnt lgkmcnt(0)
	v_add_f32_e32 v214, v214, v149
	ds_write_b32 v147, v214 offset:768
	s_or_b64 exec, exec, s[16:17]
	ds_read_b32 v149, v147 offset:2048
	s_waitcnt vmcnt(14)
	v_pk_add_f32 v[168:169], v[62:63], v[168:169]
	v_pk_add_f32 v[166:167], v[60:61], v[166:167]
	v_pk_add_f32 v[172:173], v[58:59], v[172:173]
	v_pk_add_f32 v[170:171], v[56:57], v[170:171]
	v_cvt_pk_bf16_f32 v206, v166, v167
	v_cvt_pk_bf16_f32 v207, v168, v169
	v_cvt_pk_bf16_f32 v208, v170, v171
	v_cvt_pk_bf16_f32 v209, v172, v173
	s_mov_b64 s[98:99], 0x40000
	v_lshl_add_u64 v[204:205], v[142:143], 0, s[98:99]
	global_store_dwordx4 v[204:205], v[206:209], off
	v_mul_f32_e32 v167, v167, v167
	v_mul_f32_e32 v169, v169, v169
	v_mul_f32_e32 v171, v171, v171
	v_fmac_f32_e32 v167, v166, v166
	v_fmac_f32_e32 v169, v168, v168
	v_mul_f32_e32 v173, v173, v173
	v_fmac_f32_e32 v171, v170, v170
	v_add_f32_e32 v167, v167, v169
	v_fmac_f32_e32 v173, v172, v172
	v_add_f32_e32 v167, v167, v171
	v_add_f32_e32 v214, v173, v167
	s_waitcnt vmcnt(13)
; #define PG8_LAS __attribute__((address_space(3)))
; __device__ __forceinline__ unsigned cvt_pk_bf16(float lo, float hi) { const f32x2c v = {lo, hi}; const bf16x2c b = __builtin_convertvector(v, bf16x2c); return __builtin_bit_cast(unsigned, b); }
;     __device__ __forceinline__ void operator()(const f32x4 (&acc)[2][2][4][2], const Unit& u, int wr, int wc, int fr, int fq) const {
;     ...
;             for (int m = 0; m < 4; ++m) { const size_t ro = (size_t)(row0 + ai * HALF + m * 16) * D + col0; float q = 0.f;
; #pragma unroll
;                 for (int bj = 0; bj < 2; ++bj) { const f32x4 v0 = acc[ai][bj][m][0] + *(const f32x4*)(R + ro + bj * HALF), v1 = acc[ai][bj][m][1] + *(const f32x4*)(R + ro + bj * HALF + 4);
;                     q += (v0[0] * v0[0] + v0[1] * v0[1]) + (v0[2] * v0[2] + v0[3] * v0[3]) + (v1[0] * v1[0] + v1[1] * v1[1]) + (v1[2] * v1[2] + v1[3] * v1[3]);
;                     u32x4 w; w.x = cvt_pk_bf16(v0[0], v0[1]); w.y = cvt_pk_bf16(v0[2], v0[3]); w.z = cvt_pk_bf16(v1[0], v1[1]); w.w = cvt_pk_bf16(v1[2], v1[3]);
;                     *(u32x4*)(O + ro + bj * HALF) = w; }
;                 q = rows_sum4(q);
;                 if (fq == 0) { PG8_LAS float* sp = ss + (ai * HALF + wr * 64 + m * 16 + fr) * 4 + wc; *sp += q; } }
	v_pk_add_f32 v[176:177], v[54:55], v[176:177]
	v_pk_add_f32 v[174:175], v[52:53], v[174:175]
	v_pk_add_f32 v[180:181], v[50:51], v[180:181]
	v_pk_add_f32 v[178:179], v[48:49], v[178:179]
	v_cvt_pk_bf16_f32 v210, v174, v175
	v_cvt_pk_bf16_f32 v211, v176, v177
	v_cvt_pk_bf16_f32 v212, v178, v179
	v_cvt_pk_bf16_f32 v213, v180, v181
	global_store_dwordx4 v[204:205], v[210:213], off offset:256
	v_mul_f32_e32 v175, v175, v175
	v_mul_f32_e32 v177, v177, v177
	v_mul_f32_e32 v179, v179, v179
	v_fmac_f32_e32 v175, v174, v174
	v_fmac_f32_e32 v177, v176, v176
	v_mul_f32_e32 v181, v181, v181
	v_fmac_f32_e32 v179, v178, v178
	v_add_f32_e32 v175, v175, v177
	v_fmac_f32_e32 v181, v180, v180
	v_add_f32_e32 v175, v175, v179
	v_add_f32_e32 v215, v181, v175
	v_add_f32_e32 v214, v214, v215
	s_mov_b64 s[98:99], 0xb0000
	v_lshl_add_u64 v[202:203], v[140:141], 0, s[98:99]
	global_load_dwordx4 v[166:169], v[202:203], off nt
	global_load_dwordx4 v[170:173], v[202:203], off offset:16 nt
	global_load_dwordx4 v[174:177], v[202:203], off offset:512 nt
	global_load_dwordx4 v[178:181], v[202:203], off offset:528 nt
	v_mov_b32_e32 v215, v214
	s_nop 1
	v_permlane16_swap_b32_e32 v214, v215
	v_add_f32_e32 v214, v214, v215
	v_mov_b32_e32 v215, v214
	s_nop 1
	v_permlane32_swap_b32_e32 v214, v215
	s_and_saveexec_b64 s[16:17], s[2:3]
	v_add_f32_e32 v214, v214, v215
	s_waitcnt lgkmcnt(0)
	v_add_f32_e32 v214, v214, v149
	ds_write_b32 v147, v214 offset:2048
	s_or_b64 exec, exec, s[16:17]
	ds_read_b32 v149, v147 offset:2304
	s_waitcnt vmcnt(14)
	v_pk_add_f32 v[184:185], v[46:47], v[184:185]
	v_pk_add_f32 v[182:183], v[44:45], v[182:183]
	v_pk_add_f32 v[188:189], v[42:43], v[188:189]
	v_pk_add_f32 v[186:187], v[40:41], v[186:187]
	v_cvt_pk_bf16_f32 v206, v182, v183
	v_cvt_pk_bf16_f32 v207, v184, v185
	v_cvt_pk_bf16_f32 v208, v186, v187
	v_cvt_pk_bf16_f32 v209, v188, v189
	s_mov_b64 s[98:99], 0x48000
	v_lshl_add_u64 v[204:205], v[142:143], 0, s[98:99]
	global_store_dwordx4 v[204:205], v[206:209], off
	v_mul_f32_e32 v183, v183, v183
	v_mul_f32_e32 v185, v185, v185
	v_mul_f32_e32 v187, v187, v187
	v_fmac_f32_e32 v183, v182, v182
	v_fmac_f32_e32 v185, v184, v184
	v_mul_f32_e32 v189, v189, v189
	v_fmac_f32_e32 v187, v186, v186
	v_add_f32_e32 v183, v183, v185
	v_fmac_f32_e32 v189, v188, v188
	v_add_f32_e32 v183, v183, v187
	v_add_f32_e32 v214, v189, v183
	s_waitcnt vmcnt(13)
	v_pk_add_f32 v[192:193], v[38:39], v[192:193]
	v_pk_add_f32 v[190:191], v[36:37], v[190:191]
	v_pk_add_f32 v[200:201], v[34:35], v[200:201]
	v_pk_add_f32 v[198:199], v[32:33], v[198:199]
	v_cvt_pk_bf16_f32 v210, v190, v191
	v_cvt_pk_bf16_f32 v211, v192, v193
	v_cvt_pk_bf16_f32 v212, v198, v199
	v_cvt_pk_bf16_f32 v213, v200, v201
	global_store_dwordx4 v[204:205], v[210:213], off offset:256
	v_mul_f32_e32 v191, v191, v191
	v_mul_f32_e32 v193, v193, v193
	v_mul_f32_e32 v199, v199, v199
	v_fmac_f32_e32 v191, v190, v190
	v_fmac_f32_e32 v193, v192, v192
	v_mul_f32_e32 v201, v201, v201
	v_fmac_f32_e32 v199, v198, v198
	v_add_f32_e32 v191, v191, v193
	v_fmac_f32_e32 v201, v200, v200
	v_add_f32_e32 v191, v191, v199
	v_add_f32_e32 v215, v201, v191
	v_add_f32_e32 v214, v214, v215
	v_mov_b32_e32 v215, v214
	s_nop 1
	v_permlane16_swap_b32_e32 v214, v215
	v_add_f32_e32 v214, v214, v215
	v_mov_b32_e32 v215, v214
	s_nop 1
	v_permlane32_swap_b32_e32 v214, v215
	s_and_saveexec_b64 s[16:17], s[2:3]
	v_add_f32_e32 v214, v214, v215
	s_waitcnt lgkmcnt(0)
	v_add_f32_e32 v214, v214, v149
	ds_write_b32 v147, v214 offset:2304
	s_or_b64 exec, exec, s[16:17]
	ds_read_b32 v149, v147 offset:2560
	s_waitcnt vmcnt(10)
; #define PG8_LAS __attribute__((address_space(3)))
; __device__ __forceinline__ unsigned cvt_pk_bf16(float lo, float hi) { const f32x2c v = {lo, hi}; const bf16x2c b = __builtin_convertvector(v, bf16x2c); return __builtin_bit_cast(unsigned, b); }
;     __device__ __forceinline__ void operator()(const f32x4 (&acc)[2][2][4][2], const Unit& u, int wr, int wc, int fr, int fq) const {
;     ...
;             for (int m = 0; m < 4; ++m) { const size_t ro = (size_t)(row0 + ai * HALF + m * 16) * D + col0; float q = 0.f;
; #pragma unroll
;                 for (int bj = 0; bj < 2; ++bj) { const f32x4 v0 = acc[ai][bj][m][0] + *(const f32x4*)(R + ro + bj * HALF), v1 = acc[ai][bj][m][1] + *(const f32x4*)(R + ro + bj * HALF + 4);
;                     q += (v0[0] * v0[0] + v0[1] * v0[1]) + (v0[2] * v0[2] + v0[3] * v0[3]) + (v1[0] * v1[0] + v1[1] * v1[1]) + (v1[2] * v1[2] + v1[3] * v1[3]);
;                     u32x4 w; w.x = cvt_pk_bf16(v0[0], v0[1]); w.y = cvt_pk_bf16(v0[2], v0[3]); w.z = cvt_pk_bf16(v1[0], v1[1]); w.w = cvt_pk_bf16(v1[2], v1[3]);
;                     *(u32x4*)(O + ro + bj * HALF) = w; }
;                 q = rows_sum4(q);
;                 if (fq == 0) { PG8_LAS float* sp = ss + (ai * HALF + wr * 64 + m * 16 + fr) * 4 + wc; *sp += q; } }
	v_pk_add_f32 v[152:153], v[30:31], v[152:153]
	v_pk_add_f32 v[150:151], v[28:29], v[150:151]
	v_pk_add_f32 v[156:157], v[26:27], v[156:157]
	v_pk_add_f32 v[154:155], v[24:25], v[154:155]
	v_cvt_pk_bf16_f32 v206, v150, v151
	v_cvt_pk_bf16_f32 v207, v152, v153
	v_cvt_pk_bf16_f32 v208, v154, v155
	v_cvt_pk_bf16_f32 v209, v156, v157
	s_mov_b64 s[98:99], 0x50000
	v_lshl_add_u64 v[204:205], v[142:143], 0, s[98:99]
	global_store_dwordx4 v[204:205], v[206:209], off
	v_mul_f32_e32 v151, v151, v151
	v_mul_f32_e32 v153, v153, v153
	v_mul_f32_e32 v155, v155, v155
	v_fmac_f32_e32 v151, v150, v150
	v_fmac_f32_e32 v153, v152, v152
	v_mul_f32_e32 v157, v157, v157
	v_fmac_f32_e32 v155, v154, v154
	v_add_f32_e32 v151, v151, v153
	v_fmac_f32_e32 v157, v156, v156
	v_add_f32_e32 v151, v151, v155
	v_add_f32_e32 v214, v157, v151
	s_waitcnt vmcnt(9)
	v_pk_add_f32 v[160:161], v[22:23], v[160:161]
	v_pk_add_f32 v[158:159], v[20:21], v[158:159]
	v_pk_add_f32 v[164:165], v[18:19], v[164:165]
	v_pk_add_f32 v[162:163], v[16:17], v[162:163]
	v_cvt_pk_bf16_f32 v210, v158, v159
	v_cvt_pk_bf16_f32 v211, v160, v161
	v_cvt_pk_bf16_f32 v212, v162, v163
	v_cvt_pk_bf16_f32 v213, v164, v165
	global_store_dwordx4 v[204:205], v[210:213], off offset:256
	v_mul_f32_e32 v159, v159, v159
	v_mul_f32_e32 v161, v161, v161
	v_mul_f32_e32 v163, v163, v163
	v_fmac_f32_e32 v159, v158, v158
	v_fmac_f32_e32 v161, v160, v160
	v_mul_f32_e32 v165, v165, v165
	v_fmac_f32_e32 v163, v162, v162
	v_add_f32_e32 v159, v159, v161
	v_fmac_f32_e32 v165, v164, v164
	v_add_f32_e32 v159, v159, v163
	v_add_f32_e32 v215, v165, v159
	v_add_f32_e32 v214, v214, v215
	v_mov_b32_e32 v215, v214
	s_nop 1
	v_permlane16_swap_b32_e32 v214, v215
	v_add_f32_e32 v214, v214, v215
	v_mov_b32_e32 v215, v214
	s_nop 1
	v_permlane32_swap_b32_e32 v214, v215
	s_and_saveexec_b64 s[16:17], s[2:3]
	v_add_f32_e32 v214, v214, v215
	s_waitcnt lgkmcnt(0)
	v_add_f32_e32 v214, v214, v149
	ds_write_b32 v147, v214 offset:2560
	s_or_b64 exec, exec, s[16:17]
	ds_read_b32 v149, v147 offset:2816
	s_waitcnt vmcnt(6)
	v_pk_add_f32 v[168:169], v[14:15], v[168:169]
	v_pk_add_f32 v[166:167], v[12:13], v[166:167]
	v_pk_add_f32 v[172:173], v[10:11], v[172:173]
	v_pk_add_f32 v[170:171], v[8:9], v[170:171]
	v_cvt_pk_bf16_f32 v206, v166, v167
	v_cvt_pk_bf16_f32 v207, v168, v169
	v_cvt_pk_bf16_f32 v208, v170, v171
	v_cvt_pk_bf16_f32 v209, v172, v173
	s_mov_b64 s[98:99], 0x58000
	v_lshl_add_u64 v[204:205], v[142:143], 0, s[98:99]
	global_store_dwordx4 v[204:205], v[206:209], off
	v_mul_f32_e32 v167, v167, v167
	v_mul_f32_e32 v169, v169, v169
	v_mul_f32_e32 v171, v171, v171
	v_fmac_f32_e32 v167, v166, v166
	v_fmac_f32_e32 v169, v168, v168
	v_mul_f32_e32 v173, v173, v173
	v_fmac_f32_e32 v171, v170, v170
	v_add_f32_e32 v167, v167, v169
	v_fmac_f32_e32 v173, v172, v172
	v_add_f32_e32 v167, v167, v171
	v_add_f32_e32 v214, v173, v167
	s_waitcnt vmcnt(5)
	v_pk_add_f32 v[176:177], v[6:7], v[176:177]
	v_pk_add_f32 v[174:175], v[4:5], v[174:175]
	v_pk_add_f32 v[180:181], v[2:3], v[180:181]
	v_pk_add_f32 v[178:179], v[0:1], v[178:179]
	v_cvt_pk_bf16_f32 v210, v174, v175
	v_cvt_pk_bf16_f32 v211, v176, v177
	v_cvt_pk_bf16_f32 v212, v178, v179
	v_cvt_pk_bf16_f32 v213, v180, v181
	global_store_dwordx4 v[204:205], v[210:213], off offset:256
	v_mul_f32_e32 v175, v175, v175
	v_mul_f32_e32 v177, v177, v177
	v_mul_f32_e32 v179, v179, v179
	v_fmac_f32_e32 v175, v174, v174
	v_fmac_f32_e32 v177, v176, v176
	v_mul_f32_e32 v181, v181, v181
	v_fmac_f32_e32 v179, v178, v178
	v_add_f32_e32 v175, v175, v177
	v_fmac_f32_e32 v181, v180, v180
	v_add_f32_e32 v175, v175, v179
	v_add_f32_e32 v215, v181, v175
	v_add_f32_e32 v214, v214, v215
	v_mov_b32_e32 v215, v214
	s_nop 1
	v_permlane16_swap_b32_e32 v214, v215
	v_add_f32_e32 v214, v214, v215
	v_mov_b32_e32 v215, v214
	s_nop 1
	v_permlane32_swap_b32_e32 v214, v215
	s_and_saveexec_b64 s[16:17], s[2:3]
	v_add_f32_e32 v214, v214, v215
	s_waitcnt lgkmcnt(0)
	v_add_f32_e32 v214, v214, v149
	ds_write_b32 v147, v214 offset:2816
	s_or_b64 exec, exec, s[16:17]
	s_cmp_eq_u32 s61, 3
	s_mov_b64 s[16:17], -1
	s_cbranch_scc1 .LBB0_2032
	s_andn2_b64 vcc, exec, s[4:5]
	s_cbranch_vccnz .LBB0_2031
	s_barrier
	s_branch .LBB0_2031
